# v028 + attention unit header store drain replaced by a nop (same code placement as v028)
# speedup vs baseline: 1.0047x; 1.0047x over previous
.LBB0_1410:
	s_ashr_i32 s2, s71, 8
	s_lshl_b32 s1, s71, 8
	s_lshl_b32 s0, s2, 12
	s_and_b32 s1, s1, 0xf00
	s_bfe_u32 s72, s71, 0x40004
	s_or_b32 s34, s0, s1
	s_lshl_b32 s66, s72, 9
	s_ashr_i32 s35, s34, 31
	s_mul_i32 s1, s34, 0x1800
	s_mul_hi_i32 s0, s34, 0x1800
	s_add_u32 s1, s25, s1
	s_addc_u32 s3, s38, s0
	s_mul_i32 s0, s72, 0x180
	s_nop 0
	v_mov_b32_e32 v12, v0
	s_add_u32 s0, s1, s0
	s_addc_u32 s1, s3, 0
	v_ashrrev_i32_e32 v13, 6, v12
	v_and_b32_e32 v155, 31, v12
	v_lshlrev_b32_e32 v158, 5, v13
	s_waitcnt lgkmcnt(0)
	v_bfe_u32 v176, v12, 5, 1
	v_or_b32_e32 v4, v158, v155
	v_mov_b64_e32 v[2:3], s[0:1]
	v_mad_i64_i32 v[2:3], s[0:1], v4, s45, v[2:3]
	v_lshlrev_b32_e32 v156, 4, v176
	v_lshl_add_u64 v[10:11], v[2:3], 0, v[156:157]
	global_load_dwordx4 v[2:5], v[10:11], off offset:320
	global_load_dwordx4 v[6:9], v[10:11], off offset:352
	global_load_dwordx4 v[134:137], v[10:11], off
	global_load_dwordx4 v[130:133], v[10:11], off offset:32
	global_load_dwordx4 v[126:129], v[10:11], off offset:64
	global_load_dwordx4 v[122:125], v[10:11], off offset:96
	global_load_dwordx4 v[118:121], v[10:11], off offset:128
	global_load_dwordx4 v[114:117], v[10:11], off offset:160
	global_load_dwordx4 v[110:113], v[10:11], off offset:192
	global_load_dwordx4 v[106:109], v[10:11], off offset:224
	global_load_dwordx4 v[102:105], v[10:11], off offset:256
	global_load_dwordx4 v[98:101], v[10:11], off offset:288
	s_mulk_i32 s2, 0x1100
	s_ashr_i32 s3, s2, 31
	s_lshl_b64 s[0:1], s[2:3], 13
	s_add_u32 s4, s39, s0
	s_addc_u32 s5, s40, s1
	s_add_u32 s36, s4, s66
	s_addc_u32 s37, s5, 0
	s_lshl_b64 s[4:5], s[2:3], 7
	v_lshlrev_b32_e32 v59, 3, v12
	v_readfirstlane_b32 s67, v13
	s_add_u32 s2, s41, s4
	v_and_b32_e32 v52, 63, v12
	v_mul_lo_u32 v16, v13, s45
	v_and_b32_e32 v13, 24, v59
	s_addc_u32 s3, s42, s5
	s_lshl_b32 s33, s67, 3
	s_lshl_b32 s64, s67, 2
	v_lshlrev_b32_e32 v64, 4, v52
	v_add_u32_e32 v16, s47, v16
	v_and_or_b32 v56, v12, 32, v13
	v_lshl_or_b32 v13, s67, 6, v52
	s_and_b32 s73, s33, -16
	s_and_b32 s74, s64, 4
	v_bfe_u32 v15, v12, 4, 2
	v_lshrrev_b32_e32 v14, 1, v12
	v_add_u32_e32 v180, v16, v64
	v_lshlrev_b32_e32 v16, 3, v13
	v_lshrrev_b32_e32 v13, 4, v13
	s_cmp_lg_u32 0, -1
	v_and_b32_e32 v54, 8, v14
	v_lshlrev_b32_e32 v14, 12, v15
	v_xor_b32_e32 v13, v13, v12
	v_or3_b32 v11, v15, s33, 4
	s_cselect_b32 s75, 0, 0
	s_lshl_b32 s33, s67, 11
	v_and_b32_e32 v17, 15, v12
	v_bitop3_b32 v18, v15, v12, 15 bitop3:0x78
	v_lshrrev_b32_e32 v19, 3, v12
	v_and_b32_e32 v19, 8, v19
	v_xor_b32_e32 v18, v18, v19
	v_lshl_or_b32 v55, s67, 15, v14
	v_lshlrev_b32_e32 v13, 3, v13
	s_cmp_lg_u32 s49, -1
	v_bfe_u32 v53, v12, 2, 2
	v_lshl_or_b32 v14, v18, 3, v55
	v_and_b32_e32 v57, 56, v13
	v_bitop3_b32 v13, v11, v17, 15 bitop3:0x6c
	s_cselect_b32 s64, s49, 0
	v_mov_b32_e32 v15, v157
	v_or3_b32 v10, v54, v53, s73
	v_lshlrev_b32_e32 v58, 3, v13
	s_add_i32 s76, s33, s64
	s_add_i32 s64, s33, s75
	s_lshl_b32 s65, s67, 10
	v_lshlrev_b64 v[50:51], 1, v[14:15]
	v_or_b32_e32 v10, s74, v10
	v_lshl_or_b32 v18, v11, 12, v58
	s_cmp_lg_u32 s50, -1
	s_mov_b32 m0, s76
	v_mov_b32_e32 v19, v157
	v_lshl_or_b32 v10, v10, 12, v56
	s_cselect_b32 s77, s50, 0
	v_mov_b32_e32 v11, v157
	v_and_or_b32 v16, v16, s48, v57
	s_add_i32 s77, s65, s77
	s_waitcnt vmcnt(11)
	ds_write_b128 v180, v[2:5]
	s_waitcnt vmcnt(10)
	ds_write_b128 v180, v[6:9] offset:1024
	v_lshl_add_u64 v[2:3], s[36:37], 0, v[50:51]
	global_load_lds_dwordx4 v[2:3], off
	v_lshlrev_b64 v[2:3], 1, v[18:19]
	v_lshl_add_u64 v[4:5], s[36:37], 0, v[2:3]
	s_add_i32 m0, s76, 0x400
	v_mov_b32_e32 v17, v157
	v_lshlrev_b64 v[6:7], 1, v[10:11]
	global_load_lds_dwordx4 v[4:5], off
	v_lshl_add_u64 v[4:5], v[16:17], 1, s[2:3]
	s_mov_b32 m0, s77
	v_lshl_add_u64 v[8:9], s[36:37], 0, v[6:7]
	s_mov_b64 s[2:3], 0x100
	v_or_b32_e32 v20, 64, v10
	global_load_lds_dwordx4 v[4:5], off
	v_lshl_add_u64 v[10:11], v[8:9], 0, s[2:3]
	s_mov_b32 m0, s64
	s_mov_b64 s[2:3], 0x180
	global_load_lds_dwordx4 v[10:11], off
	s_add_i32 m0, s64, 0x400
	v_lshl_add_u64 v[8:9], v[8:9], 0, s[2:3]
	s_add_u32 s2, s36, 0x80000
	s_addc_u32 s3, s37, 0
	global_load_lds_dwordx4 v[8:9], off
	v_lshl_add_u64 v[8:9], s[2:3], 0, v[50:51]
	s_add_i32 m0, s76, 0x4000
	v_lshl_add_u64 v[2:3], s[2:3], 0, v[2:3]
	global_load_lds_dwordx4 v[8:9], off
	s_add_i32 m0, s76, 0x4400
	s_mov_b64 s[2:3], 0x2000
	global_load_lds_dwordx4 v[2:3], off
	s_add_i32 m0, s77, 0x2000
	v_lshl_add_u64 v[2:3], v[4:5], 0, s[2:3]
	s_add_u32 s2, s36, 0x80100
	s_addc_u32 s3, s37, 0
	v_mov_b32_e32 v21, v157
	global_load_lds_dwordx4 v[2:3], off
	v_lshl_add_u64 v[2:3], s[2:3], 0, v[6:7]
	s_add_i32 m0, s64, 0x4000
	v_lshlrev_b32_e32 v10, 8, v155
	global_load_lds_dwordx4 v[2:3], off
	v_lshl_add_u64 v[2:3], v[20:21], 1, s[2:3]
	s_add_i32 m0, s64, 0x4400
	v_or_b32_e32 v13, 32, v156
	global_load_lds_dwordx4 v[2:3], off
	v_lshlrev_b32_e32 v2, 4, v12
	v_and_b32_e32 v11, 0xf0, v2
	v_bitop3_b32 v182, v156, v10, v11 bitop3:0xde
	v_add_u32_e32 v183, 0, v182
	s_waitcnt vmcnt(0)
	s_waitcnt vmcnt(0) lgkmcnt(0)
	s_barrier
	ds_read_b128 v[2:5], v183 offset:49152
	ds_read_b128 v[6:9], v183 offset:57344
	s_waitcnt lgkmcnt(1)
	v_mfma_f32_32x32x16_bf16 v[34:49], v[2:5], v[134:137], 0
	v_bitop3_b32 v184, v13, v10, v11 bitop3:0xde
	v_add_u32_e32 v185, 0, v184
	v_or_b32_e32 v14, 64, v156
	v_bitop3_b32 v186, v14, v10, v11 bitop3:0xde
	v_add_u32_e32 v187, 0, v186
	v_or_b32_e32 v65, 0x60, v156
	v_bitop3_b32 v188, v65, v10, v11 bitop3:0xde
	s_waitcnt lgkmcnt(0)
	v_mfma_f32_32x32x16_bf16 v[18:33], v[6:9], v[134:137], 0
	ds_read_b128 v[2:5], v185 offset:49152
	ds_read_b128 v[6:9], v185 offset:57344
	v_add_u32_e32 v189, 0, v188
	v_cmp_gt_u32_e64 s[2:3], 32, v52
	s_mov_b32 s36, -1
	s_mov_b32 s37, 0
	v_mov_b32_e32 v178, 0
	s_waitcnt lgkmcnt(1)
	v_mfma_f32_32x32x16_bf16 v[34:49], v[2:5], v[130:133], v[34:49]
	s_waitcnt lgkmcnt(0)
	v_mfma_f32_32x32x16_bf16 v[18:33], v[6:9], v[130:133], v[18:33]
	ds_read_b128 v[2:5], v187 offset:49152
	ds_read_b128 v[6:9], v187 offset:57344
	s_waitcnt lgkmcnt(1)
	v_mfma_f32_32x32x16_bf16 v[34:49], v[2:5], v[126:129], v[34:49]
	s_waitcnt lgkmcnt(0)
	v_mfma_f32_32x32x16_bf16 v[18:33], v[6:9], v[126:129], v[18:33]
	ds_read_b128 v[2:5], v189 offset:49152
	ds_read_b128 v[6:9], v189 offset:57344
	s_waitcnt lgkmcnt(1)
	v_mfma_f32_32x32x16_bf16 v[34:49], v[2:5], v[122:125], v[34:49]
	v_or_b32_e32 v2, 0x80, v156
	v_bitop3_b32 v190, v2, v10, v11 bitop3:0xde
	v_add_u32_e32 v191, 0, v190
	s_waitcnt lgkmcnt(0)
	v_mfma_f32_32x32x16_bf16 v[18:33], v[6:9], v[122:125], v[18:33]
	ds_read_b128 v[2:5], v191 offset:49152
	ds_read_b128 v[6:9], v191 offset:57344
	s_waitcnt lgkmcnt(1)
	v_mfma_f32_32x32x16_bf16 v[34:49], v[2:5], v[118:121], v[34:49]
	v_or_b32_e32 v2, 0xa0, v156
	v_bitop3_b32 v192, v2, v10, v11 bitop3:0xde
	v_add_u32_e32 v193, 0, v192
	s_waitcnt lgkmcnt(0)
	v_mfma_f32_32x32x16_bf16 v[18:33], v[6:9], v[118:121], v[18:33]
	ds_read_b128 v[2:5], v193 offset:49152
	ds_read_b128 v[6:9], v193 offset:57344
	s_waitcnt lgkmcnt(1)
	v_mfma_f32_32x32x16_bf16 v[34:49], v[2:5], v[114:117], v[34:49]
	v_or_b32_e32 v2, 0xc0, v156
	v_bitop3_b32 v194, v2, v10, v11 bitop3:0xde
	v_add_u32_e32 v195, 0, v194
	s_waitcnt lgkmcnt(0)
	v_mfma_f32_32x32x16_bf16 v[18:33], v[6:9], v[114:117], v[18:33]
	ds_read_b128 v[2:5], v195 offset:49152
	ds_read_b128 v[6:9], v195 offset:57344
	s_waitcnt lgkmcnt(1)
	v_mfma_f32_32x32x16_bf16 v[34:49], v[2:5], v[110:113], v[34:49]
	v_or_b32_e32 v2, 0xe0, v156
	v_bitop3_b32 v196, v2, v10, v11 bitop3:0xde
	v_add_u32_e32 v197, 0, v196
	v_lshlrev_b32_e32 v10, 7, v155
	v_and_b32_e32 v11, 0x70, v59
	v_bitop3_b32 v199, v156, v10, v11 bitop3:0xde
	v_add_u32_e32 v200, s50, v199
	s_waitcnt lgkmcnt(0)
	v_mfma_f32_32x32x16_bf16 v[18:33], v[6:9], v[110:113], v[18:33]
	ds_read_b128 v[2:5], v197 offset:49152
	ds_read_b128 v[6:9], v197 offset:57344
	v_bitop3_b32 v201, v13, v10, v11 bitop3:0xde
	v_add_u32_e32 v202, s50, v201
	v_bitop3_b32 v203, v14, v10, v11 bitop3:0xde
	v_add_u32_e32 v204, s50, v203
	v_bitop3_b32 v205, v65, v10, v11 bitop3:0xde
	v_add_u32_e32 v206, s50, v205
	s_waitcnt lgkmcnt(1)
	v_mfma_f32_32x32x16_bf16 v[34:49], v[2:5], v[106:109], v[34:49]
	v_lshlrev_b32_e32 v59, 3, v52
	s_waitcnt lgkmcnt(0)
	v_mfma_f32_32x32x16_bf16 v[18:33], v[6:9], v[106:109], v[18:33]
	ds_read_b128 v[2:5], v200
	ds_read_b128 v[6:9], v200 offset:4096
	s_waitcnt lgkmcnt(1)
	v_mfma_f32_32x32x16_bf16 v[34:49], v[2:5], v[102:105], v[34:49]
	s_waitcnt lgkmcnt(0)
	v_mfma_f32_32x32x16_bf16 v[18:33], v[6:9], v[102:105], v[18:33]
	ds_read_b128 v[2:5], v202
	ds_read_b128 v[6:9], v202 offset:4096
	s_waitcnt lgkmcnt(1)
	v_mfma_f32_32x32x16_bf16 v[34:49], v[2:5], v[98:101], v[34:49]
	s_waitcnt lgkmcnt(0)
	v_mfma_f32_32x32x16_bf16 v[18:33], v[6:9], v[98:101], v[18:33]
	ds_read_b128 v[2:5], v204
	ds_read_b128 v[6:9], v180
	ds_read_b128 v[14:17], v204 offset:4096
	ds_read_b128 v[60:63], v180 offset:1024
	s_waitcnt lgkmcnt(2)
	v_mfma_f32_32x32x16_bf16 v[34:49], v[2:5], v[6:9], v[34:49]
	ds_read_b128 v[2:5], v206
	s_waitcnt lgkmcnt(2)
	v_mfma_f32_32x32x16_bf16 v[18:33], v[14:17], v[6:9], v[18:33]
	v_and_b32_e32 v6, 0x3fffffc0, v12
	v_lshl_add_u32 v159, v6, 2, s46
	v_and_b32_e32 v6, 0xc0, v64
	ds_read_b128 v[64:67], v206 offset:4096
	v_lshl_add_u32 v177, v155, 2, v159
	s_waitcnt lgkmcnt(0)
	s_barrier
	v_mfma_f32_32x32x16_bf16 v[34:49], v[2:5], v[60:63], v[34:49]
	v_lshlrev_b32_e32 v3, 1, v12
	v_and_or_b32 v2, v59, 24, v6
	v_and_b32_e32 v3, 32, v3
	v_and_b32_e32 v4, 0x100, v59
	v_or3_b32 v179, v2, v3, v4
	v_mov_b64_e32 v[2:3], s[8:9]
	v_mov_b64_e32 v[16:17], s[22:23]
	v_mfma_f32_32x32x16_bf16 v[18:33], v[64:67], v[60:63], v[18:33]
	s_nop 3
	v_max_f32_e32 v60, v35, v35
	v_max_f32_e32 v61, v34, v34
	v_max_f32_e32 v60, v61, v60
	v_max3_f32 v60, v60, v36, v37
	v_max3_f32 v60, v60, v38, v39
	v_max3_f32 v60, v60, v40, v41
	v_max3_f32 v60, v60, v42, v43
	v_max3_f32 v60, v60, v44, v45
	v_max3_f32 v60, v60, v46, v47
	v_max3_f32 v60, v60, v48, v49
	v_max3_f32 v60, v60, v18, v19
	v_max3_f32 v60, v60, v20, v21
	v_max3_f32 v60, v60, v22, v23
	v_max3_f32 v60, v60, v24, v25
	v_max3_f32 v60, v60, v26, v27
	v_max3_f32 v60, v60, v28, v29
	v_max3_f32 v60, v60, v30, v31
	v_max3_f32 v60, v60, v32, v33
	v_mov_b32_e32 v61, v60
	s_nop 1
	v_permlane32_swap_b32_e32 v60, v61
	v_max_f32_e32 v61, v61, v61
	v_max_f32_e32 v60, v60, v60
	v_max_f32_e32 v60, v60, v61
	v_add_f32_e32 v61, 0x7149f2ca, v60
	v_max_f32_e32 v60, 0xf149f2ca, v60
	v_cmp_ge_f32_e32 vcc, s51, v61
	v_sub_f32_e32 v61, 0xf149f2ca, v60
	v_mul_f32_e32 v61, 0x3dd53b94, v61
	v_exp_f32_e32 v61, v61
	s_cmp_eq_u64 vcc, exec
	s_cselect_b64 vcc, -1, 0
	v_cndmask_b32_e32 v208, v60, v1, vcc
	v_mul_f32_e32 v60, 0xbdd53b94, v208
	v_cndmask_b32_e64 v207, v61, 1.0, vcc
	v_mov_b32_e32 v61, v60
	v_fmac_f32_e32 v61, 0x3dd53b94, v49
	v_pk_fma_f32 v[152:153], v[18:19], s[24:25], v[60:61] op_sel_hi:[1,0,0]
	v_lshl_or_b32 v18, s67, 9, v59
	v_and_or_b32 v18, v18, s48, v57
	v_mov_b32_e32 v19, v157
	v_lshl_add_u64 v[160:161], v[18:19], 1, s[4:5]
	v_or_b32_e32 v18, s73, v54
	v_fmamk_f32 v34, v34, 0x3dd53b94, v60
	v_fmamk_f32 v35, v35, 0x3dd53b94, v60
	v_fmamk_f32 v36, v36, 0x3dd53b94, v60
	v_fmamk_f32 v37, v37, 0x3dd53b94, v60
	v_fmamk_f32 v38, v38, 0x3dd53b94, v60
	v_fmamk_f32 v39, v39, 0x3dd53b94, v60
	v_fmamk_f32 v40, v40, 0x3dd53b94, v60
	v_fmamk_f32 v41, v41, 0x3dd53b94, v60
	v_fmamk_f32 v42, v42, 0x3dd53b94, v60
	v_fmamk_f32 v43, v43, 0x3dd53b94, v60
	v_fmamk_f32 v44, v44, 0x3dd53b94, v60
	v_fmamk_f32 v45, v45, 0x3dd53b94, v60
	v_fmamk_f32 v46, v46, 0x3dd53b94, v60
	v_fmamk_f32 v47, v47, 0x3dd53b94, v60
	v_fmamk_f32 v48, v48, 0x3dd53b94, v60
	v_or3_b32 v18, v18, s74, v53
	v_exp_f32_e32 v239, v34
	v_exp_f32_e32 v241, v35
	v_exp_f32_e32 v237, v36
	v_exp_f32_e32 v240, v37
	v_exp_f32_e32 v236, v38
	v_exp_f32_e32 v238, v39
	v_exp_f32_e32 v234, v40
	v_exp_f32_e32 v235, v41
	v_exp_f32_e32 v231, v42
	v_exp_f32_e32 v233, v43
	v_exp_f32_e32 v230, v44
	v_exp_f32_e32 v232, v45
	v_exp_f32_e32 v227, v46
	v_exp_f32_e32 v229, v47
	v_exp_f32_e32 v226, v48
	v_exp_f32_e32 v228, v61
	s_or_b32 s0, s0, s66
	v_lshl_or_b32 v18, v18, 12, v56
	s_movk_i32 s4, 0x4000
	v_lshl_add_u64 v[162:163], v[18:19], 1, s[0:1]
	v_or3_b32 v18, v55, v58, s4
	v_mov_b64_e32 v[4:5], s[10:11]
	v_mov_b64_e32 v[6:7], s[12:13]
	v_mov_b64_e32 v[8:9], s[14:15]
	v_mov_b64_e32 v[10:11], s[16:17]
	v_mov_b64_e32 v[12:13], s[18:19]
	v_mov_b64_e32 v[14:15], s[20:21]
	v_pk_fma_f32 v[138:139], v[32:33], s[24:25], v[60:61] op_sel_hi:[1,0,0]
	v_pk_fma_f32 v[140:141], v[30:31], s[24:25], v[60:61] op_sel_hi:[1,0,0]
	v_pk_fma_f32 v[142:143], v[28:29], s[24:25], v[60:61] op_sel_hi:[1,0,0]
	v_pk_fma_f32 v[144:145], v[26:27], s[24:25], v[60:61] op_sel_hi:[1,0,0]
	v_pk_fma_f32 v[146:147], v[24:25], s[24:25], v[60:61] op_sel_hi:[1,0,0]
	v_pk_fma_f32 v[148:149], v[22:23], s[24:25], v[60:61] op_sel_hi:[1,0,0]
	v_pk_fma_f32 v[150:151], v[20:21], s[24:25], v[60:61] op_sel_hi:[1,0,0]
	v_lshl_add_u64 v[164:165], s[0:1], 0, v[50:51]
	v_lshl_add_u64 v[166:167], v[18:19], 1, s[0:1]
	v_mov_b64_e32 v[64:65], v[16:17]
	v_mov_b64_e32 v[48:49], v[16:17]
	v_mov_b64_e32 v[32:33], v[16:17]
	v_add_u32_e32 v181, s75, v179
	v_mov_b64_e32 v[62:63], v[14:15]
	v_mov_b64_e32 v[60:61], v[12:13]
	v_mov_b64_e32 v[58:59], v[10:11]
	v_mov_b64_e32 v[56:57], v[8:9]
	v_mov_b64_e32 v[54:55], v[6:7]
	v_mov_b64_e32 v[52:53], v[4:5]
	v_mov_b64_e32 v[50:51], v[2:3]
	v_mov_b64_e32 v[46:47], v[14:15]
	v_mov_b64_e32 v[44:45], v[12:13]
	v_mov_b64_e32 v[42:43], v[10:11]
	v_mov_b64_e32 v[40:41], v[8:9]
	v_mov_b64_e32 v[38:39], v[6:7]
	v_mov_b64_e32 v[36:37], v[4:5]
	v_mov_b64_e32 v[34:35], v[2:3]
	v_mov_b64_e32 v[30:31], v[14:15]
	v_mov_b64_e32 v[28:29], v[12:13]
	v_mov_b64_e32 v[26:27], v[10:11]
	v_mov_b64_e32 v[24:25], v[8:9]
	v_mov_b64_e32 v[22:23], v[6:7]
	v_mov_b64_e32 v[20:21], v[4:5]
	v_mov_b64_e32 v[18:19], v[2:3]
	s_mov_b32 s66, 2
